# same stack; per-wave kscale rows now reloaded whenever the item's k-block changes (independent of grid size)
# baseline (speedup 1.0000x reference)
.LBB0_8:
	s_or_b64 exec, exec, s[2:3]
	s_ashr_i32 s0, s0, 6
	s_lshl_b32 s1, s82, 3
	s_add_i32 s14, s0, s1
	s_waitcnt lgkmcnt(0)
	s_add_u32 s18, s12, 0x1a00000
	s_addc_u32 s19, s13, 0
	s_lshl_b32 s80, s88, 3
	s_mov_b32 s60, 0
	s_mov_b32 s61, -1
	s_cmp_gt_i32 s14, 0xc4ff
	v_and_b32_e32 v36, 63, v37
	v_writelane_b32 v254, s1, 5
	s_cbranch_scc1 .LBB0_31
	s_add_u32 s1, s12, 0x1c00000
	s_addc_u32 s2, s13, 0
	v_lshlrev_b32_e32 v1, 4, v36
	s_add_u32 s3, s12, 0x5c00000
	s_mul_i32 s4, s0, 0x2100
	v_and_b32_e32 v10, 48, v1
	s_addc_u32 s11, s13, 0
	s_add_i32 s4, s4, 0
	v_mul_u32_u24_e32 v1, 0x84, v10
	v_and_b32_e32 v3, 60, v36
	v_add3_u32 v7, s4, v1, v3
	v_lshlrev_b32_e32 v1, 2, v36
	v_lshrrev_b32_e32 v5, 2, v36
	v_and_b32_e32 v1, 0x80, v1
	v_and_or_b32 v9, v5, 7, v1
	v_lshlrev_b32_e32 v1, 3, v36
	v_lshrrev_b32_e32 v24, 3, v36
	v_and_b32_e32 v1, 56, v1
	v_and_b32_e32 v6, 31, v37
	v_mov_b32_e32 v13, 0
	v_mul_u32_u24_e32 v3, 0x84, v1
	v_lshlrev_b32_e32 v12, 1, v1
	v_lshlrev_b32_e32 v1, 2, v24
	v_lshrrev_b32_e32 v4, 5, v36
	v_lshl_add_u32 v8, v6, 2, s4
	v_add3_u32 v25, s4, v3, v1
	v_lshl_add_u64 v[16:17], s[12:13], 0, v[12:13]
	s_mov_b64 s[4:5], 0x1600000
	s_mov_b32 s9, 0
	s_movk_i32 s15, 0x84
	v_mov_b32_e32 v11, v13
	v_or_b32_e32 v21, 16, v5
	v_lshl_add_u64 v[14:15], s[18:19], 0, v[12:13]
	v_or_b32_e32 v26, 8, v24
	v_or_b32_e32 v27, 16, v24
	v_or_b32_e32 v28, 24, v24
	v_lshl_add_u64 v[16:17], v[16:17], 0, s[4:5]
	v_mov_b32_e32 v1, v4
	s_brev_b32 s10, 34
	s_movk_i32 s24, 0x7fff
	s_mov_b32 s25, 0xffff0000
	v_mov_b32_e32 v29, 0x2000
	s_mov_b32 s26, s14
	s_branch .LBB0_11

.LBB0_20:
	v_readfirstlane_b32 s56, v18
	v_readfirstlane_b32 s57, v19
	s_lshl_b32 s51, s6, 13
	s_add_u32 s56, s56, s51
	s_addc_u32 s57, s57, 0
	s_lshl_b32 s52, s6, 2
	s_add_u32 s52, s4, s52
	s_addc_u32 s53, s5, 0
	v_and_b32_e32 v100, 3, v36
	v_lshrrev_b32_e32 v101, 5, v36
	v_lshl_or_b32 v100, v101, 2, v100
	v_bfe_u32 v101, v36, 2, 3
	v_lshlrev_b32_e32 v102, 13, v100
	v_lshl_or_b32 v102, v101, 4, v102
	v_lshlrev_b32_e32 v104, 2, v100
	v_lshlrev_b32_e32 v103, 2, v6
	v_sub_u32_e32 v103, v8, v103
	v_mad_u32_u24 v103, v100, s15, v103
	v_lshl_add_u32 v103, v101, 4, v103
	s_cmp_eq_u32 s6, s61
	s_cbranch_scc1 .Lks_done
	global_load_dword v152, v104, s[52:53] offset:0
	global_load_dword v153, v104, s[52:53] offset:32
	global_load_dword v154, v104, s[52:53] offset:64
	global_load_dword v155, v104, s[52:53] offset:96
	global_load_dword v156, v104, s[52:53] offset:128
	global_load_dword v157, v104, s[52:53] offset:160
	global_load_dword v158, v104, s[52:53] offset:192
	global_load_dword v159, v104, s[52:53] offset:224
	s_waitcnt vmcnt(0)
	s_mov_b32 s61, s6
